# attention passes: static s_setprio 1 for waves 0-3 during each pass; plus previous changes
# speedup vs baseline: 1.0077x; 1.0077x over previous
; #define LAS __attribute__((address_space(3)))
; __device__ __forceinline__ unsigned cvt_pk_bf16(float lo, float hi) { unsigned r; asm volatile("v_cvt_pk_bf16_f32 %0, %1, %2" : "=v"(r) : "v"(lo), "v"(hi)); return r; }
; __device__ __forceinline__ float bf_lo(unsigned w) { return __uint_as_float(w << 16); }
; __device__ __forceinline__ float bf_hi(unsigned w) { return __uint_as_float(w & 0xffff0000u); }
;     __device__ __forceinline__ bf16_t* proj() const { return (bf16_t*)(ws + WS_PROJ); }
; template <bool ROBUST>
; __device__ __forceinline__ bool attn_pass(const bf16_t* __restrict__ proj, LAS char* lds, int qrow0, int ctxrow0, int latrow0, int NT, int h, int comp, f32x16 (&o)[4]) {
;     int tid = threadIdx.x; asm volatile("" : "+v"(tid));
;     const int wid = tid >> 6, lane = tid & 63, r32 = lane & 31, hi = lane >> 5;
;     LAS char* V_lds = lds + OFF_V; LAS char* K_lds = lds + OFF_K;
;     LAS float* ws = (LAS float*)(lds + OFF_WS) + wid * 64; LAS float* li_l = ws; LAS float* al_l = ws + 32;
;     float m_reg = 0.f, l_reg = 0.f;
; #pragma unroll
;     for (int d = 0; d < 4; ++d) o[d] = f32x16{};
;     bf16x8 qr[4];
;     { const bf16_t* Qw = proj + (size_t)(qrow0 + wid * 32 + r32) * INW + C_Q + h * 128 + comp * 64 + hi * 8;
; #pragma unroll
;       for (int d0 = 0; d0 < 4; ++d0) {
;           const u32x4 w = *(const u32x4*)(Qw + d0 * 16); constexpr float C = SCALE * 1.4426950408889634f; u32x4 s;
;           s.x = cvt_pk_bf16(bf_lo(w.x) * C, bf_hi(w.x) * C); s.y = cvt_pk_bf16(bf_lo(w.y) * C, bf_hi(w.y) * C); s.z = cvt_pk_bf16(bf_lo(w.z) * C, bf_hi(w.z) * C); s.w = cvt_pk_bf16(bf_lo(w.w) * C, bf_hi(w.w) * C);
;           qr[d0] = *reinterpret_cast<bf16x8*>(&s); } }
.LBB0_348:
	v_mov_b32_e32 v195, v0
	v_mov_b32_e32 v171, v147
	v_ashrrev_i32_e32 v8, 6, v195
	v_and_b32_e32 v194, 31, v195
	v_lshlrev_b32_e32 v2, 5, v8
	v_add3_u32 v2, v194, s30, v2
	v_ashrrev_i32_e32 v3, 31, v2
	v_lshlrev_b64 v[2:3], 13, v[2:3]
	v_bfe_u32 v4, v195, 5, 1
	v_lshl_add_u64 v[2:3], s[68:69], 0, v[2:3]
	v_lshl_add_u64 v[2:3], s[76:77], 1, v[2:3]
	v_lshlrev_b32_e32 v170, 4, v4
	v_lshl_add_u64 v[2:3], v[2:3], 0, v[170:171]
	global_load_dwordx4 v[48:51], v[2:3], off
	global_load_dwordx4 v[36:39], v[2:3], off offset:32
	global_load_dwordx4 v[40:43], v[2:3], off offset:64
	global_load_dwordx4 v[44:47], v[2:3], off offset:96
	v_lshlrev_b32_e32 v34, 3, v195
	s_ashr_i32 s67, s66, 31
	s_lshl_b64 s[24:25], s[66:67], 13
	v_readfirstlane_b32 s40, v8
	s_nop 3
	s_cmp_ge_u32 s40, 4
	s_cbranch_scc1 .Lat_prio_skip
	s_setprio 1
